# P3 uin tiles: hand-written pipelined tile loop (4-row strips, weights loaded once, ds_write_b128 transpose, next tile loads before the LDS/store phase)
# baseline (speedup 1.0000x reference)
.LBB0_469:
	s_cmpk_gt_i32 s92, 0x3ff
	v_readlane_b32 s56, v252, 59
	s_cbranch_scc1 .LBB0_506
	s_and_b32 s0, s62, 3
	s_cmp_lg_u32 s0, 0
	s_cbranch_scc1 .Luin_orig
	v_readlane_b32 s2, v252, 4
	v_readlane_b32 s3, v252, 5
	v_readlane_b32 s8, v252, 39
	v_readlane_b32 s9, v252, 40
	v_readlane_b32 s10, v252, 60
	v_readlane_b32 s11, v252, 61
	s_add_u32 s4, s2, 0x1eb00000
	s_addc_u32 s5, s3, 0
	s_add_u32 s6, s2, 0x2f700000
	s_addc_u32 s7, s3, 0
	s_mov_b32 s12, s92
	s_movk_i32 s27, 0x4000
	v_and_b32_e32 v1, 31, v0
	v_lshrrev_b32_e32 v2, 5, v0
	s_and_b32 s14, s12, 3
	s_lshl_b32 s14, s14, 8
	v_lshl_add_u32 v5, v1, 3, s14
	v_lshlrev_b32_e32 v5, 2, v5
	s_add_u32 s36, s8, 0x1000
	s_addc_u32 s37, s9, 0
	global_load_dwordx4 v[8:11], v5, s[36:37]
	global_load_dwordx4 v[12:15], v5, s[36:37] offset:16
	s_add_u32 s36, s8, 0x4000
	s_addc_u32 s37, s9, 0
	global_load_dwordx4 v[16:19], v5, s[36:37]
	global_load_dwordx4 v[20:23], v5, s[36:37] offset:16
	s_add_u32 s36, s8, 0x7000
	s_addc_u32 s37, s9, 0
	global_load_dwordx4 v[24:27], v5, s[36:37]
	global_load_dwordx4 v[28:31], v5, s[36:37] offset:16
	s_add_u32 s36, s10, 0x1000
	s_addc_u32 s37, s11, 0
	global_load_dwordx4 v[32:35], v5, s[36:37]
	global_load_dwordx4 v[36:39], v5, s[36:37] offset:16
	s_add_u32 s36, s8, 0x2000
	s_addc_u32 s37, s9, 0
	global_load_dwordx4 v[40:43], v5, s[36:37]
	global_load_dwordx4 v[44:47], v5, s[36:37] offset:16
	s_add_u32 s36, s8, 0x5000
	s_addc_u32 s37, s9, 0
	global_load_dwordx4 v[48:51], v5, s[36:37]
	global_load_dwordx4 v[52:55], v5, s[36:37] offset:16
	s_add_u32 s36, s8, 0x8000
	s_addc_u32 s37, s9, 0
	global_load_dwordx4 v[56:59], v5, s[36:37]
	global_load_dwordx4 v[60:63], v5, s[36:37] offset:16
	s_add_u32 s36, s10, 0x2000
	s_addc_u32 s37, s11, 0
	global_load_dwordx4 v[64:67], v5, s[36:37]
	global_load_dwordx4 v[68:71], v5, s[36:37] offset:16
	v_mul_u32_u24_e32 v6, 0x880, v1
	v_lshl_add_u32 v6, v2, 4, v6
	v_lshrrev_b32_e32 v126, 4, v0
	v_and_b32_e32 v127, 15, v0
	v_mul_u32_u24_e32 v7, 0x110, v126
	v_lshl_add_u32 v7, v127, 4, v7
	v_lshlrev_b32_e32 v164, 16, v126
	v_lshl_add_u32 v164, v127, 4, v164
	s_movk_i32 s26, 0x3200
	s_lshl_b32 s15, s14, 1
	s_add_u32 s15, s15, 0x2040
	s_lshr_b32 s13, s12, 2
	s_lshl_b32 s13, s13, 6
	v_lshl_add_u32 v3, v2, 2, s13
	v_add_u32_e32 v4, 4, v3
	v_add_u32_e32 v3, -1, v3
	v_mul_lo_u32 v165, v3, s26
	v_lshl_add_u32 v126, v1, 4, s15
	v_add_u32_e32 v165, v165, v126
	v_add_u32_e32 v166, 0x3200, v165
	v_add_u32_e32 v167, 0x3200, v166
	v_add_u32_e32 v168, 0x3200, v167
	v_add_u32_e32 v169, 0x3200, v168
	v_add_u32_e32 v170, 0x3200, v169
	v_mov_b32_e32 v72, 0
	v_mov_b32_e32 v73, 0
	v_mov_b32_e32 v74, 0
	v_mov_b32_e32 v75, 0
	v_mov_b32_e32 v92, 0
	v_mov_b32_e32 v93, 0
	v_mov_b32_e32 v94, 0
	v_mov_b32_e32 v95, 0
	v_mov_b32_e32 v96, 0
	v_mov_b32_e32 v97, 0
	v_mov_b32_e32 v98, 0
	v_mov_b32_e32 v99, 0
	v_mov_b32_e32 v116, 0
	v_mov_b32_e32 v117, 0
	v_mov_b32_e32 v118, 0
	v_mov_b32_e32 v119, 0
	global_load_dwordx4 v[76:79], v166, s[4:5]
	global_load_dwordx4 v[100:103], v166, s[4:5] offset:2048
	global_load_dwordx4 v[80:83], v167, s[4:5]
	global_load_dwordx4 v[104:107], v167, s[4:5] offset:2048
	global_load_dwordx4 v[84:87], v168, s[4:5]
	global_load_dwordx4 v[108:111], v168, s[4:5] offset:2048
	global_load_dwordx4 v[88:91], v169, s[4:5]
	global_load_dwordx4 v[112:115], v169, s[4:5] offset:2048
	v_cmp_le_i32_e32 vcc, 0, v3
	s_and_saveexec_b64 s[22:23], vcc
	global_load_dwordx4 v[72:75], v165, s[4:5]
	global_load_dwordx4 v[96:99], v165, s[4:5] offset:2048
	s_mov_b64 exec, s[22:23]
	v_cmp_gt_i32_e32 vcc, s27, v4
	s_and_saveexec_b64 s[22:23], vcc
	global_load_dwordx4 v[92:95], v170, s[4:5]
	global_load_dwordx4 v[116:119], v170, s[4:5] offset:2048
	s_mov_b64 exec, s[22:23]
	s_waitcnt vmcnt(0)
	s_branch .Luin_have
.Luin_tile:
	s_waitcnt vmcnt(8)
.Luin_have:
	v_lshlrev_b32_e32 v120, 16, v72
	v_lshlrev_b32_e32 v121, 16, v76
	v_lshlrev_b32_e32 v122, 16, v80
	v_lshlrev_b32_e32 v123, 16, v84
	v_lshlrev_b32_e32 v124, 16, v88
	v_lshlrev_b32_e32 v125, 16, v92
	v_mul_f32_e32 v126, v16, v121
	v_fmac_f32_e32 v126, v8, v120
	v_fmac_f32_e32 v126, v24, v122
	v_add_f32_e32 v132, v32, v126
	v_mul_f32_e32 v127, v16, v122
	v_fmac_f32_e32 v127, v8, v121
	v_fmac_f32_e32 v127, v24, v123
	v_add_f32_e32 v133, v32, v127
	v_mul_f32_e32 v128, v16, v123
	v_fmac_f32_e32 v128, v8, v122
	v_fmac_f32_e32 v128, v24, v124
	v_add_f32_e32 v134, v32, v128
	v_mul_f32_e32 v129, v16, v124
	v_fmac_f32_e32 v129, v8, v123
	v_fmac_f32_e32 v129, v24, v125
	v_add_f32_e32 v135, v32, v129
	v_and_b32_e32 v120, 0xffff0000, v72
	v_and_b32_e32 v121, 0xffff0000, v76
	v_and_b32_e32 v122, 0xffff0000, v80
	v_and_b32_e32 v123, 0xffff0000, v84
	v_and_b32_e32 v124, 0xffff0000, v88
	v_and_b32_e32 v125, 0xffff0000, v92
	v_mul_f32_e32 v126, v17, v121
	v_fmac_f32_e32 v126, v9, v120
	v_fmac_f32_e32 v126, v25, v122
	v_add_f32_e32 v136, v33, v126
	v_mul_f32_e32 v127, v17, v122
	v_fmac_f32_e32 v127, v9, v121
	v_fmac_f32_e32 v127, v25, v123
	v_add_f32_e32 v137, v33, v127
	v_mul_f32_e32 v128, v17, v123
	v_fmac_f32_e32 v128, v9, v122
	v_fmac_f32_e32 v128, v25, v124
	v_add_f32_e32 v138, v33, v128
	v_mul_f32_e32 v129, v17, v124
	v_fmac_f32_e32 v129, v9, v123
	v_fmac_f32_e32 v129, v25, v125
	v_add_f32_e32 v139, v33, v129
	v_lshlrev_b32_e32 v120, 16, v73
	v_lshlrev_b32_e32 v121, 16, v77
	v_lshlrev_b32_e32 v122, 16, v81
	v_lshlrev_b32_e32 v123, 16, v85
	v_lshlrev_b32_e32 v124, 16, v89
	v_lshlrev_b32_e32 v125, 16, v93
	v_mul_f32_e32 v126, v18, v121
	v_fmac_f32_e32 v126, v10, v120
	v_fmac_f32_e32 v126, v26, v122
	v_add_f32_e32 v140, v34, v126
	v_mul_f32_e32 v127, v18, v122
	v_fmac_f32_e32 v127, v10, v121
	v_fmac_f32_e32 v127, v26, v123
	v_add_f32_e32 v141, v34, v127
	v_mul_f32_e32 v128, v18, v123
	v_fmac_f32_e32 v128, v10, v122
	v_fmac_f32_e32 v128, v26, v124
	v_add_f32_e32 v142, v34, v128
	v_mul_f32_e32 v129, v18, v124
	v_fmac_f32_e32 v129, v10, v123
	v_fmac_f32_e32 v129, v26, v125
	v_add_f32_e32 v143, v34, v129
	v_and_b32_e32 v120, 0xffff0000, v73
	v_and_b32_e32 v121, 0xffff0000, v77
	v_and_b32_e32 v122, 0xffff0000, v81
	v_and_b32_e32 v123, 0xffff0000, v85
	v_and_b32_e32 v124, 0xffff0000, v89
	v_and_b32_e32 v125, 0xffff0000, v93
	v_mul_f32_e32 v126, v19, v121
	v_fmac_f32_e32 v126, v11, v120
	v_fmac_f32_e32 v126, v27, v122
	v_add_f32_e32 v144, v35, v126
	v_mul_f32_e32 v127, v19, v122
	v_fmac_f32_e32 v127, v11, v121
	v_fmac_f32_e32 v127, v27, v123
	v_add_f32_e32 v145, v35, v127
	v_mul_f32_e32 v128, v19, v123
	v_fmac_f32_e32 v128, v11, v122
	v_fmac_f32_e32 v128, v27, v124
	v_add_f32_e32 v146, v35, v128
	v_mul_f32_e32 v129, v19, v124
	v_fmac_f32_e32 v129, v11, v123
	v_fmac_f32_e32 v129, v27, v125
	v_add_f32_e32 v147, v35, v129
	v_lshlrev_b32_e32 v120, 16, v74
	v_lshlrev_b32_e32 v121, 16, v78
	v_lshlrev_b32_e32 v122, 16, v82
	v_lshlrev_b32_e32 v123, 16, v86
	v_lshlrev_b32_e32 v124, 16, v90
	v_lshlrev_b32_e32 v125, 16, v94
	v_mul_f32_e32 v126, v20, v121
	v_fmac_f32_e32 v126, v12, v120
	v_fmac_f32_e32 v126, v28, v122
	v_add_f32_e32 v148, v36, v126
	v_mul_f32_e32 v127, v20, v122
	v_fmac_f32_e32 v127, v12, v121
	v_fmac_f32_e32 v127, v28, v123
	v_add_f32_e32 v149, v36, v127
	v_mul_f32_e32 v128, v20, v123
	v_fmac_f32_e32 v128, v12, v122
	v_fmac_f32_e32 v128, v28, v124
	v_add_f32_e32 v150, v36, v128
	v_mul_f32_e32 v129, v20, v124
	v_fmac_f32_e32 v129, v12, v123
	v_fmac_f32_e32 v129, v28, v125
	v_add_f32_e32 v151, v36, v129
	v_and_b32_e32 v120, 0xffff0000, v74
	v_and_b32_e32 v121, 0xffff0000, v78
	v_and_b32_e32 v122, 0xffff0000, v82
	v_and_b32_e32 v123, 0xffff0000, v86
	v_and_b32_e32 v124, 0xffff0000, v90
	v_and_b32_e32 v125, 0xffff0000, v94
	v_mul_f32_e32 v126, v21, v121
	v_fmac_f32_e32 v126, v13, v120
	v_fmac_f32_e32 v126, v29, v122
	v_add_f32_e32 v152, v37, v126
	v_mul_f32_e32 v127, v21, v122
	v_fmac_f32_e32 v127, v13, v121
	v_fmac_f32_e32 v127, v29, v123
	v_add_f32_e32 v153, v37, v127
	v_mul_f32_e32 v128, v21, v123
	v_fmac_f32_e32 v128, v13, v122
	v_fmac_f32_e32 v128, v29, v124
	v_add_f32_e32 v154, v37, v128
	v_mul_f32_e32 v129, v21, v124
	v_fmac_f32_e32 v129, v13, v123
	v_fmac_f32_e32 v129, v29, v125
	v_add_f32_e32 v155, v37, v129
	v_lshlrev_b32_e32 v120, 16, v75
	v_lshlrev_b32_e32 v121, 16, v79
	v_lshlrev_b32_e32 v122, 16, v83
	v_lshlrev_b32_e32 v123, 16, v87
	v_lshlrev_b32_e32 v124, 16, v91
	v_lshlrev_b32_e32 v125, 16, v95
	v_mul_f32_e32 v126, v22, v121
	v_fmac_f32_e32 v126, v14, v120
	v_fmac_f32_e32 v126, v30, v122
	v_add_f32_e32 v156, v38, v126
	v_mul_f32_e32 v127, v22, v122
	v_fmac_f32_e32 v127, v14, v121
	v_fmac_f32_e32 v127, v30, v123
	v_add_f32_e32 v157, v38, v127
	v_mul_f32_e32 v128, v22, v123
	v_fmac_f32_e32 v128, v14, v122
	v_fmac_f32_e32 v128, v30, v124
	v_add_f32_e32 v158, v38, v128
	v_mul_f32_e32 v129, v22, v124
	v_fmac_f32_e32 v129, v14, v123
	v_fmac_f32_e32 v129, v30, v125
	v_add_f32_e32 v159, v38, v129
	v_and_b32_e32 v120, 0xffff0000, v75
	v_and_b32_e32 v121, 0xffff0000, v79
	v_and_b32_e32 v122, 0xffff0000, v83
	v_and_b32_e32 v123, 0xffff0000, v87
	v_and_b32_e32 v124, 0xffff0000, v91
	v_and_b32_e32 v125, 0xffff0000, v95
	v_mul_f32_e32 v126, v23, v121
	v_fmac_f32_e32 v126, v15, v120
	v_fmac_f32_e32 v126, v31, v122
	v_add_f32_e32 v160, v39, v126
	v_mul_f32_e32 v127, v23, v122
	v_fmac_f32_e32 v127, v15, v121
	v_fmac_f32_e32 v127, v31, v123
	v_add_f32_e32 v161, v39, v127
	v_mul_f32_e32 v128, v23, v123
	v_fmac_f32_e32 v128, v15, v122
	v_fmac_f32_e32 v128, v31, v124
	v_add_f32_e32 v162, v39, v128
	v_mul_f32_e32 v129, v23, v124
	v_fmac_f32_e32 v129, v15, v123
	v_fmac_f32_e32 v129, v31, v125
	v_add_f32_e32 v163, v39, v129
	v_lshlrev_b32_e32 v120, 16, v96
	v_lshlrev_b32_e32 v121, 16, v100
	v_lshlrev_b32_e32 v122, 16, v104
	v_lshlrev_b32_e32 v123, 16, v108
	v_lshlrev_b32_e32 v124, 16, v112
	v_lshlrev_b32_e32 v125, 16, v116
	v_mul_f32_e32 v126, v48, v121
	v_fmac_f32_e32 v126, v40, v120
	v_fmac_f32_e32 v126, v56, v122
	v_add_f32_e32 v126, v64, v126
	v_mul_f32_e32 v132, v132, v126
	v_mul_f32_e32 v127, v48, v122
	v_fmac_f32_e32 v127, v40, v121
	v_fmac_f32_e32 v127, v56, v123
	v_add_f32_e32 v127, v64, v127
	v_mul_f32_e32 v133, v133, v127
	v_mul_f32_e32 v128, v48, v123
	v_fmac_f32_e32 v128, v40, v122
	v_fmac_f32_e32 v128, v56, v124
	v_add_f32_e32 v128, v64, v128
	v_mul_f32_e32 v134, v134, v128
	v_mul_f32_e32 v129, v48, v124
	v_fmac_f32_e32 v129, v40, v123
	v_fmac_f32_e32 v129, v56, v125
	v_add_f32_e32 v129, v64, v129
	v_mul_f32_e32 v135, v135, v129
	v_and_b32_e32 v120, 0xffff0000, v96
	v_and_b32_e32 v121, 0xffff0000, v100
	v_and_b32_e32 v122, 0xffff0000, v104
	v_and_b32_e32 v123, 0xffff0000, v108
	v_and_b32_e32 v124, 0xffff0000, v112
	v_and_b32_e32 v125, 0xffff0000, v116
	v_mul_f32_e32 v126, v49, v121
	v_fmac_f32_e32 v126, v41, v120
	v_fmac_f32_e32 v126, v57, v122
	v_add_f32_e32 v126, v65, v126
	v_mul_f32_e32 v136, v136, v126
	v_mul_f32_e32 v127, v49, v122
	v_fmac_f32_e32 v127, v41, v121
	v_fmac_f32_e32 v127, v57, v123
	v_add_f32_e32 v127, v65, v127
	v_mul_f32_e32 v137, v137, v127
	v_mul_f32_e32 v128, v49, v123
	v_fmac_f32_e32 v128, v41, v122
	v_fmac_f32_e32 v128, v57, v124
	v_add_f32_e32 v128, v65, v128
	v_mul_f32_e32 v138, v138, v128
	v_mul_f32_e32 v129, v49, v124
	v_fmac_f32_e32 v129, v41, v123
	v_fmac_f32_e32 v129, v57, v125
	v_add_f32_e32 v129, v65, v129
	v_mul_f32_e32 v139, v139, v129
	v_lshlrev_b32_e32 v120, 16, v97
	v_lshlrev_b32_e32 v121, 16, v101
	v_lshlrev_b32_e32 v122, 16, v105
	v_lshlrev_b32_e32 v123, 16, v109
	v_lshlrev_b32_e32 v124, 16, v113
	v_lshlrev_b32_e32 v125, 16, v117
	v_mul_f32_e32 v126, v50, v121
	v_fmac_f32_e32 v126, v42, v120
	v_fmac_f32_e32 v126, v58, v122
	v_add_f32_e32 v126, v66, v126
	v_mul_f32_e32 v140, v140, v126
	v_mul_f32_e32 v127, v50, v122
	v_fmac_f32_e32 v127, v42, v121
	v_fmac_f32_e32 v127, v58, v123
	v_add_f32_e32 v127, v66, v127
	v_mul_f32_e32 v141, v141, v127
	v_mul_f32_e32 v128, v50, v123
	v_fmac_f32_e32 v128, v42, v122
	v_fmac_f32_e32 v128, v58, v124
	v_add_f32_e32 v128, v66, v128
	v_mul_f32_e32 v142, v142, v128
	v_mul_f32_e32 v129, v50, v124
	v_fmac_f32_e32 v129, v42, v123
	v_fmac_f32_e32 v129, v58, v125
	v_add_f32_e32 v129, v66, v129
	v_mul_f32_e32 v143, v143, v129
	v_and_b32_e32 v120, 0xffff0000, v97
	v_and_b32_e32 v121, 0xffff0000, v101
	v_and_b32_e32 v122, 0xffff0000, v105
	v_and_b32_e32 v123, 0xffff0000, v109
	v_and_b32_e32 v124, 0xffff0000, v113
	v_and_b32_e32 v125, 0xffff0000, v117
	v_mul_f32_e32 v126, v51, v121
	v_fmac_f32_e32 v126, v43, v120
	v_fmac_f32_e32 v126, v59, v122
	v_add_f32_e32 v126, v67, v126
	v_mul_f32_e32 v144, v144, v126
	v_mul_f32_e32 v127, v51, v122
	v_fmac_f32_e32 v127, v43, v121
	v_fmac_f32_e32 v127, v59, v123
	v_add_f32_e32 v127, v67, v127
	v_mul_f32_e32 v145, v145, v127
	v_mul_f32_e32 v128, v51, v123
	v_fmac_f32_e32 v128, v43, v122
	v_fmac_f32_e32 v128, v59, v124
	v_add_f32_e32 v128, v67, v128
	v_mul_f32_e32 v146, v146, v128
	v_mul_f32_e32 v129, v51, v124
	v_fmac_f32_e32 v129, v43, v123
	v_fmac_f32_e32 v129, v59, v125
	v_add_f32_e32 v129, v67, v129
	v_mul_f32_e32 v147, v147, v129
	v_lshlrev_b32_e32 v120, 16, v98
	v_lshlrev_b32_e32 v121, 16, v102
	v_lshlrev_b32_e32 v122, 16, v106
	v_lshlrev_b32_e32 v123, 16, v110
	v_lshlrev_b32_e32 v124, 16, v114
	v_lshlrev_b32_e32 v125, 16, v118
	v_mul_f32_e32 v126, v52, v121
	v_fmac_f32_e32 v126, v44, v120
	v_fmac_f32_e32 v126, v60, v122
	v_add_f32_e32 v126, v68, v126
	v_mul_f32_e32 v148, v148, v126
	v_mul_f32_e32 v127, v52, v122
	v_fmac_f32_e32 v127, v44, v121
	v_fmac_f32_e32 v127, v60, v123
	v_add_f32_e32 v127, v68, v127
	v_mul_f32_e32 v149, v149, v127
	v_mul_f32_e32 v128, v52, v123
	v_fmac_f32_e32 v128, v44, v122
	v_fmac_f32_e32 v128, v60, v124
	v_add_f32_e32 v128, v68, v128
	v_mul_f32_e32 v150, v150, v128
	v_mul_f32_e32 v129, v52, v124
	v_fmac_f32_e32 v129, v44, v123
	v_fmac_f32_e32 v129, v60, v125
	v_add_f32_e32 v129, v68, v129
	v_mul_f32_e32 v151, v151, v129
	v_and_b32_e32 v120, 0xffff0000, v98
	v_and_b32_e32 v121, 0xffff0000, v102
	v_and_b32_e32 v122, 0xffff0000, v106
	v_and_b32_e32 v123, 0xffff0000, v110
	v_and_b32_e32 v124, 0xffff0000, v114
	v_and_b32_e32 v125, 0xffff0000, v118
	v_mul_f32_e32 v126, v53, v121
	v_fmac_f32_e32 v126, v45, v120
	v_fmac_f32_e32 v126, v61, v122
	v_add_f32_e32 v126, v69, v126
	v_mul_f32_e32 v152, v152, v126
	v_mul_f32_e32 v127, v53, v122
	v_fmac_f32_e32 v127, v45, v121
	v_fmac_f32_e32 v127, v61, v123
	v_add_f32_e32 v127, v69, v127
	v_mul_f32_e32 v153, v153, v127
	v_mul_f32_e32 v128, v53, v123
	v_fmac_f32_e32 v128, v45, v122
	v_fmac_f32_e32 v128, v61, v124
	v_add_f32_e32 v128, v69, v128
	v_mul_f32_e32 v154, v154, v128
	v_mul_f32_e32 v129, v53, v124
	v_fmac_f32_e32 v129, v45, v123
	v_fmac_f32_e32 v129, v61, v125
	v_add_f32_e32 v129, v69, v129
	v_mul_f32_e32 v155, v155, v129
	v_lshlrev_b32_e32 v120, 16, v99
	v_lshlrev_b32_e32 v121, 16, v103
	v_lshlrev_b32_e32 v122, 16, v107
	v_lshlrev_b32_e32 v123, 16, v111
	v_lshlrev_b32_e32 v124, 16, v115
	v_lshlrev_b32_e32 v125, 16, v119
	v_mul_f32_e32 v126, v54, v121
	v_fmac_f32_e32 v126, v46, v120
	v_fmac_f32_e32 v126, v62, v122
	v_add_f32_e32 v126, v70, v126
	v_mul_f32_e32 v156, v156, v126
	v_mul_f32_e32 v127, v54, v122
	v_fmac_f32_e32 v127, v46, v121
	v_fmac_f32_e32 v127, v62, v123
	v_add_f32_e32 v127, v70, v127
	v_mul_f32_e32 v157, v157, v127
	v_mul_f32_e32 v128, v54, v123
	v_fmac_f32_e32 v128, v46, v122
	v_fmac_f32_e32 v128, v62, v124
	v_add_f32_e32 v128, v70, v128
	v_mul_f32_e32 v158, v158, v128
	v_mul_f32_e32 v129, v54, v124
	v_fmac_f32_e32 v129, v46, v123
	v_fmac_f32_e32 v129, v62, v125
	v_add_f32_e32 v129, v70, v129
	v_mul_f32_e32 v159, v159, v129
	v_and_b32_e32 v120, 0xffff0000, v99
	v_and_b32_e32 v121, 0xffff0000, v103
	v_and_b32_e32 v122, 0xffff0000, v107
	v_and_b32_e32 v123, 0xffff0000, v111
	v_and_b32_e32 v124, 0xffff0000, v115
	v_and_b32_e32 v125, 0xffff0000, v119
	v_mul_f32_e32 v126, v55, v121
	v_fmac_f32_e32 v126, v47, v120
	v_fmac_f32_e32 v126, v63, v122
	v_add_f32_e32 v126, v71, v126
	v_mul_f32_e32 v160, v160, v126
	v_mul_f32_e32 v127, v55, v122
	v_fmac_f32_e32 v127, v47, v121
	v_fmac_f32_e32 v127, v63, v123
	v_add_f32_e32 v127, v71, v127
	v_mul_f32_e32 v161, v161, v127
	v_mul_f32_e32 v128, v55, v123
	v_fmac_f32_e32 v128, v47, v122
	v_fmac_f32_e32 v128, v63, v124
	v_add_f32_e32 v128, v71, v128
	v_mul_f32_e32 v162, v162, v128
	v_mul_f32_e32 v129, v55, v124
	v_fmac_f32_e32 v129, v47, v123
	v_fmac_f32_e32 v129, v63, v125
	v_add_f32_e32 v129, v71, v129
	v_mul_f32_e32 v163, v163, v129
	s_lshr_b32 s16, s12, 2
	s_lshl_b32 s16, s16, 8
	s_lshl_b32 s17, s14, 16
	s_add_u32 s16, s16, s17
	s_add_u32 s24, s6, s16
	s_addc_u32 s25, s7, 0
	s_add_i32 s12, s12, s62
	s_cmpk_lt_i32 s12, 0x400
	s_cbranch_scc0 .Luin_nonext
	s_lshr_b32 s13, s12, 2
	s_lshl_b32 s13, s13, 6
	v_lshl_add_u32 v3, v2, 2, s13
	v_add_u32_e32 v4, 4, v3
	v_add_u32_e32 v3, -1, v3
	v_mul_lo_u32 v165, v3, s26
	v_lshl_add_u32 v126, v1, 4, s15
	v_add_u32_e32 v165, v165, v126
	v_add_u32_e32 v166, 0x3200, v165
	v_add_u32_e32 v167, 0x3200, v166
	v_add_u32_e32 v168, 0x3200, v167
	v_add_u32_e32 v169, 0x3200, v168
	v_add_u32_e32 v170, 0x3200, v169
	v_mov_b32_e32 v72, 0
	v_mov_b32_e32 v73, 0
	v_mov_b32_e32 v74, 0
	v_mov_b32_e32 v75, 0
	v_mov_b32_e32 v92, 0
	v_mov_b32_e32 v93, 0
	v_mov_b32_e32 v94, 0
	v_mov_b32_e32 v95, 0
	v_mov_b32_e32 v96, 0
	v_mov_b32_e32 v97, 0
	v_mov_b32_e32 v98, 0
	v_mov_b32_e32 v99, 0
	v_mov_b32_e32 v116, 0
	v_mov_b32_e32 v117, 0
	v_mov_b32_e32 v118, 0
	v_mov_b32_e32 v119, 0
	global_load_dwordx4 v[76:79], v166, s[4:5]
	global_load_dwordx4 v[100:103], v166, s[4:5] offset:2048
	global_load_dwordx4 v[80:83], v167, s[4:5]
	global_load_dwordx4 v[104:107], v167, s[4:5] offset:2048
	global_load_dwordx4 v[84:87], v168, s[4:5]
	global_load_dwordx4 v[108:111], v168, s[4:5] offset:2048
	global_load_dwordx4 v[88:91], v169, s[4:5]
	global_load_dwordx4 v[112:115], v169, s[4:5] offset:2048
	v_cmp_le_i32_e32 vcc, 0, v3
	s_and_saveexec_b64 s[22:23], vcc
	global_load_dwordx4 v[72:75], v165, s[4:5]
	global_load_dwordx4 v[96:99], v165, s[4:5] offset:2048
	s_mov_b64 exec, s[22:23]
	v_cmp_gt_i32_e32 vcc, s27, v4
	s_and_saveexec_b64 s[22:23], vcc
	global_load_dwordx4 v[92:95], v170, s[4:5]
	global_load_dwordx4 v[116:119], v170, s[4:5] offset:2048
	s_mov_b64 exec, s[22:23]
.Luin_nonext:
	ds_write_b128 v6, v[132:135]
	ds_write_b128 v6, v[136:139] offset:272
	ds_write_b128 v6, v[140:143] offset:544
	ds_write_b128 v6, v[144:147] offset:816
	ds_write_b128 v6, v[148:151] offset:1088
	ds_write_b128 v6, v[152:155] offset:1360
	ds_write_b128 v6, v[156:159] offset:1632
	ds_write_b128 v6, v[160:163] offset:1904
	s_waitcnt lgkmcnt(0)
	s_barrier
	ds_read_b128 v[172:175], v7
	s_waitcnt lgkmcnt(0)
	global_store_dwordx4 v164, v[172:175], s[24:25]
	s_nop 1
	s_add_u32 s24, s24, 0x200000
	s_addc_u32 s25, s25, 0
	ds_read_b128 v[172:175], v7 offset:8704
	s_waitcnt lgkmcnt(0)
	global_store_dwordx4 v164, v[172:175], s[24:25]
	s_nop 1
	s_add_u32 s24, s24, 0x200000
	s_addc_u32 s25, s25, 0
	ds_read_b128 v[172:175], v7 offset:17408
	s_waitcnt lgkmcnt(0)
	global_store_dwordx4 v164, v[172:175], s[24:25]
	s_nop 1
	s_add_u32 s24, s24, 0x200000
	s_addc_u32 s25, s25, 0
	ds_read_b128 v[172:175], v7 offset:26112
	s_waitcnt lgkmcnt(0)
	global_store_dwordx4 v164, v[172:175], s[24:25]
	s_nop 1
	s_add_u32 s24, s24, 0x200000
	s_addc_u32 s25, s25, 0
	ds_read_b128 v[172:175], v7 offset:34816
	s_waitcnt lgkmcnt(0)
	global_store_dwordx4 v164, v[172:175], s[24:25]
	s_nop 1
	s_add_u32 s24, s24, 0x200000
	s_addc_u32 s25, s25, 0
	ds_read_b128 v[172:175], v7 offset:43520
	s_waitcnt lgkmcnt(0)
	global_store_dwordx4 v164, v[172:175], s[24:25]
	s_nop 1
	s_add_u32 s24, s24, 0x200000
	s_addc_u32 s25, s25, 0
	ds_read_b128 v[172:175], v7 offset:52224
	s_waitcnt lgkmcnt(0)
	global_store_dwordx4 v164, v[172:175], s[24:25]
	s_nop 1
	s_add_u32 s24, s24, 0x200000
	s_addc_u32 s25, s25, 0
	ds_read_b128 v[172:175], v7 offset:60928
	s_waitcnt lgkmcnt(0)
	global_store_dwordx4 v164, v[172:175], s[24:25]
	s_nop 1
	s_barrier
	s_cmpk_lt_i32 s12, 0x400
	s_cbranch_scc1 .Luin_tile
	s_branch .LBB0_506
.Luin_orig:
	v_readlane_b32 s0, v252, 2
	v_lshlrev_b32_e32 v94, 4, v180
	v_mov_b32_e32 v95, 0
	v_readlane_b32 s1, v252, 3
	v_readlane_b32 s2, v252, 4
	v_readlane_b32 s3, v252, 5
	s_mov_b64 s[0:1], 0x2f700000
	s_waitcnt vmcnt(0)
	v_or_b32_e32 v9, 0xc00, v0
	v_lshl_add_u64 v[2:3], s[2:3], 0, v[94:95]
	v_lshl_add_u64 v[96:97], v[2:3], 0, s[0:1]
	s_movk_i32 s0, 0xe00
	v_lshlrev_b32_e32 v1, 3, v0
	v_or_b32_e32 v3, 0x200, v0
	v_or_b32_e32 v7, 0x600, v0
	v_or_b32_e32 v8, 0xa00, v0
	v_lshrrev_b32_e32 v114, 4, v9
	v_cmp_gt_u32_e64 s[0:1], s0, v9
	v_or_b32_e32 v9, 0xe00, v0
	v_and_b32_e32 v1, 0xf8, v1
	v_lshrrev_b32_e32 v104, 5, v0
	v_lshrrev_b32_e32 v108, 4, v0
	v_lshrrev_b32_e32 v109, 4, v3
	v_lshrrev_b32_e32 v111, 4, v7
	v_lshrrev_b32_e32 v113, 4, v8
	v_lshrrev_b32_e32 v115, 4, v9
	v_lshl_add_u32 v4, v104, 2, 0
	v_mul_u32_u24_e32 v5, 0x104, v1
	v_add_u32_e32 v6, 0, v94
	v_mul_u32_u24_e32 v2, 0x104, v108
	v_mul_u32_u24_e32 v3, 0x104, v109
	v_mul_u32_u24_e32 v7, 0x104, v111
	v_mul_u32_u24_e32 v8, 0x104, v113
	v_mul_u32_u24_e32 v10, 0x104, v114
	v_mul_u32_u24_e32 v9, 0x104, v115
	v_or_b32_e32 v105, 16, v104
	v_or_b32_e32 v106, 32, v104
	v_or_b32_e32 v107, 48, v104
	v_or_b32_e32 v110, 64, v108
	v_or_b32_e32 v112, 0x80, v108
	s_lshl_b32 s14, s92, 4
	s_lshl_b32 s15, s62, 4
	s_lshl_b32 s16, s92, 8
	s_lshl_b32 s17, s62, 8
	s_movk_i32 s22, 0x3200
	v_mov_b64_e32 v[98:99], s[20:21]
	s_movk_i32 s23, 0x3fff
	s_mov_b64 s[6:7], 0x3000
	s_movk_i32 s24, 0x3000
	s_mov_b64 s[8:9], 0x6000
	s_movk_i32 s25, 0x6000
	v_add_u32_e32 v116, v6, v2
	v_add_u32_e32 v117, v6, v3
	v_add_u32_e32 v118, v6, v7
	v_add_u32_e32 v119, v6, v8
	v_add_u32_e32 v120, v6, v10
	v_add_u32_e32 v121, v6, v9
	v_mov_b32_e32 v122, 0x1000
	v_mov_b32_e32 v123, 0x2000
	v_add_u32_e32 v124, v4, v5
	s_mov_b32 s26, s92
	s_branch .LBB0_472
